# hyena filter write-out stores marked nt (filters are read only two phases later)
# speedup vs baseline: 1.0030x; 1.0030x over previous
;     ...
;     float* HF = isctx ? (float*)(P.ws + WS_HFC) + (size_t)tid * 512 + 256 : (float*)(P.ws + WS_HF) + (size_t)tid * 32768 + LSEQ;
;     float asum = 0.f;
; #pragma unroll 1
;     for (int hp = 0; hp < 2; ++hp) {
;         float accf[16], accb[16];
; #pragma unroll
;         for (int i = 0; i < 16; ++i) { accf[i] = 0.f; accb[i] = 0.f; }
; #pragma unroll 2
;         for (int k4 = 0; k4 < 16; ++k4) {
;             float wf[4], wb[4];
; #pragma unroll
;             for (int j = 0; j < 4; ++j) { wf[j] = w3[(k4 * 4 + j) * 1024 + tid]; wb[j] = w3[(k4 * 4 + j) * 1024 + 512 + tid]; }
; #pragma unroll
;             for (int pp = 0; pp < 16; ++pp) {
;                 const float4 hv = *(const float4*)&h2[(hp * 16 + pp) * 64 + k4 * 4];
;                 accf[pp] += hv.x * wf[0]; accf[pp] += hv.y * wf[1]; accf[pp] += hv.z * wf[2]; accf[pp] += hv.w * wf[3];
;                 accb[pp] += hv.x * wb[0]; accb[pp] += hv.y * wb[1]; accb[pp] += hv.z * wb[2]; accb[pp] += hv.w * wb[3];
;             }
;         }
; #pragma unroll
;         for (int pp = 0; pp < 16; ++pp) {
;             const int pos = p0 + hp * 16 + pp;
;             const float t = (float)pos / (float)(l - 1);
;             const float win = expf(-t * delta);
;             const float f = accf[pp] * win, b = accb[pp] * win;
;             HF[pos] = f; asum += fabsf(f);
;             if (pos >= 1) { HF[-pos] = b; asum += fabsf(b); }
.Lhy_wout:
	s_and_b32 s4, s8, 16
	s_or_b32 s4, s4, s15
	s_cmpk_gt_i32 s14, 0x1ff
	s_mov_b32 s98, 0xe38000
	s_cselect_b32 s98, 0x4e28400, s98
	s_cselect_b32 s99, 11, 17
	v_readlane_b32 s100, v252, 21
	v_readlane_b32 s101, v252, 22
	v_and_b32_e32 v79, 63, v0
	v_lshrrev_b32_e32 v80, 4, v79
	v_and_b32_e32 v81, 15, v79
	v_and_b32_e32 v82, 0x1c0, v0
	v_add_u32_e32 v82, v82, v80
	v_lshlrev_b32_e32 v82, s99, v82
	v_add_u32_e32 v82, s98, v82
	v_add_u32_e32 v83, s4, v81
	v_lshl_add_u32 v84, v83, 2, v82
	v_sub_u32_e32 v85, 15, v81
	v_add_u32_e32 v85, s4, v85
	v_lshlrev_b32_e32 v86, 2, v85
	v_sub_u32_e32 v86, v82, v86
	v_cmp_ne_u32_e32 vcc, 0, v85
	s_lshl_b32 s5, 4, s99
	v_lshrrev_b32_e32 v87, 6, v0
	v_mul_u32_u24_e32 v87, 0x2100, v87
	v_mul_u32_u24_e32 v80, 0x84, v80
	v_add_u32_e32 v87, v87, v80
	v_lshl_add_u32 v87, v81, 2, v87
	v_add_u32_e32 v87, 0xa000, v87
	ds_read_b32 v26, v87 offset:0
	ds_read_b32 v27, v87 offset:528
	ds_read_b32 v28, v87 offset:1056
	ds_read_b32 v29, v87 offset:1584
	ds_read_b32 v30, v87 offset:2112
	ds_read_b32 v31, v87 offset:2640
	ds_read_b32 v32, v87 offset:3168
	ds_read_b32 v33, v87 offset:3696
	ds_read_b32 v34, v87 offset:4224
	ds_read_b32 v35, v87 offset:4752
	ds_read_b32 v36, v87 offset:5280
	ds_read_b32 v37, v87 offset:5808
	ds_read_b32 v38, v87 offset:6336
	ds_read_b32 v39, v87 offset:6864
	ds_read_b32 v40, v87 offset:7392
	ds_read_b32 v41, v87 offset:7920
	ds_read_b32 v42, v87 offset:64
	ds_read_b32 v43, v87 offset:592
	ds_read_b32 v44, v87 offset:1120
	ds_read_b32 v45, v87 offset:1648
	ds_read_b32 v46, v87 offset:2176
	ds_read_b32 v47, v87 offset:2704
	ds_read_b32 v48, v87 offset:3232
	ds_read_b32 v49, v87 offset:3760
	ds_read_b32 v50, v87 offset:4288
	ds_read_b32 v51, v87 offset:4816
	ds_read_b32 v52, v87 offset:5344
	ds_read_b32 v53, v87 offset:5872
	ds_read_b32 v54, v87 offset:6400
	ds_read_b32 v55, v87 offset:6928
	ds_read_b32 v56, v87 offset:7456
	ds_read_b32 v57, v87 offset:7984
	s_waitcnt lgkmcnt(15)
	global_store_dword v84, v26, s[100:101] nt
	v_add_u32_e32 v84, s5, v84
	global_store_dword v84, v27, s[100:101] nt
	v_add_u32_e32 v84, s5, v84
	global_store_dword v84, v28, s[100:101] nt
	v_add_u32_e32 v84, s5, v84
	global_store_dword v84, v29, s[100:101] nt
	v_add_u32_e32 v84, s5, v84
	global_store_dword v84, v30, s[100:101] nt
	v_add_u32_e32 v84, s5, v84
	global_store_dword v84, v31, s[100:101] nt
	v_add_u32_e32 v84, s5, v84
	global_store_dword v84, v32, s[100:101] nt
	v_add_u32_e32 v84, s5, v84
	global_store_dword v84, v33, s[100:101] nt
	v_add_u32_e32 v84, s5, v84
	global_store_dword v84, v34, s[100:101] nt
	v_add_u32_e32 v84, s5, v84
	global_store_dword v84, v35, s[100:101] nt
	v_add_u32_e32 v84, s5, v84
	global_store_dword v84, v36, s[100:101] nt
	v_add_u32_e32 v84, s5, v84
	global_store_dword v84, v37, s[100:101] nt
	v_add_u32_e32 v84, s5, v84
	global_store_dword v84, v38, s[100:101] nt
	v_add_u32_e32 v84, s5, v84
	global_store_dword v84, v39, s[100:101] nt
	v_add_u32_e32 v84, s5, v84
	global_store_dword v84, v40, s[100:101] nt
	v_add_u32_e32 v84, s5, v84
	global_store_dword v84, v41, s[100:101] nt
	s_waitcnt lgkmcnt(0)
	s_mov_b64 s[2:3], exec
	s_and_b64 exec, exec, vcc
	global_store_dword v86, v42, s[100:101] nt
	v_add_u32_e32 v86, s5, v86
	global_store_dword v86, v43, s[100:101] nt
	v_add_u32_e32 v86, s5, v86
	global_store_dword v86, v44, s[100:101] nt
	v_add_u32_e32 v86, s5, v86
	global_store_dword v86, v45, s[100:101] nt
	v_add_u32_e32 v86, s5, v86
	global_store_dword v86, v46, s[100:101] nt
	v_add_u32_e32 v86, s5, v86
	global_store_dword v86, v47, s[100:101] nt
	v_add_u32_e32 v86, s5, v86
	global_store_dword v86, v48, s[100:101] nt
	v_add_u32_e32 v86, s5, v86
	global_store_dword v86, v49, s[100:101] nt
	v_add_u32_e32 v86, s5, v86
	global_store_dword v86, v50, s[100:101] nt
	v_add_u32_e32 v86, s5, v86
	global_store_dword v86, v51, s[100:101] nt
	v_add_u32_e32 v86, s5, v86
	global_store_dword v86, v52, s[100:101] nt
	v_add_u32_e32 v86, s5, v86
	global_store_dword v86, v53, s[100:101] nt
	v_add_u32_e32 v86, s5, v86
	global_store_dword v86, v54, s[100:101] nt
	v_add_u32_e32 v86, s5, v86
	global_store_dword v86, v55, s[100:101] nt
	v_add_u32_e32 v86, s5, v86
	global_store_dword v86, v56, s[100:101] nt
	v_add_u32_e32 v86, s5, v86
	global_store_dword v86, v57, s[100:101] nt
	s_mov_b64 exec, s[2:3]
	s_branch .LBB0_74
